# baseline (speedup 1.0000x reference)
.Lno_anc:
	s_or_b64 exec, exec, s[8:9]
	v_mov_b32_e32 v7, 0x80
	s_waitcnt vmcnt(0)
	s_sub_u32 s26, 0x1ff, s2
	s_mul_i32 s26, s26, 7
	s_lshr_b32 s26, s26, 6
	s_cmp_eq_u32 s26, 0
	s_cbranch_scc1 .Lhold_done
